# P4: n-state scan tail of workgroup 0 rewritten with batched loads (was 32 dependent load-wait steps)
# speedup vs baseline: 1.0476x; 1.0122x over previous
.LBB0_590:
	s_or_b64 exec, exec, s[6:7]
	s_movk_i32 s2, 0x200
	v_cmp_gt_i32_e32 vcc, s2, v20
	s_and_saveexec_b64 s[2:3], vcc
	s_cbranch_execz .LBB0_593
	v_and_b32_e32 v2, 0xffffffe0, v20
	v_ashrrev_i32_e32 v3, 31, v2
	v_lshlrev_b64 v[6:7], 2, v[2:3]
	v_lshlrev_b32_e32 v2, 7, v20
	v_and_b32_e32 v2, 0xfffff000, v2
	v_ashrrev_i32_e32 v3, 31, v2
	v_and_b32_e32 v1, 31, v1
	v_lshlrev_b64 v[8:9], 2, v[2:3]
	v_lshl_or_b32 v8, v1, 4, v8
	v_mov_b32_e32 v1, 0
	s_mov_b32 s8, 32
	s_mov_b64 s[6:7], 0x800
	v_mov_b32_e32 v2, 0
	v_mov_b32_e32 v3, v1
	v_mov_b32_e32 v4, v1
	v_mov_b32_e32 v5, v1
	v_lshl_add_u64 v[40:41], s[18:19], 0, v[8:9]
	v_lshl_add_u64 v[44:45], s[18:19], 0, v[6:7]
	v_add_co_u32_e32 v42, vcc, 0x602000, v40
	s_nop 1
	v_addc_co_u32_e32 v43, vcc, 0, v41, vcc
	v_add_co_u32_e32 v40, vcc, 0x642000, v40
	s_nop 1
	v_addc_co_u32_e32 v41, vcc, 0, v41, vcc
	v_add_co_u32_e32 v44, vcc, 0x600000, v44
	s_nop 1
	v_addc_co_u32_e32 v45, vcc, 0, v45, vcc
	global_load_dword v46, v[44:45], off
	global_load_dword v54, v[44:45], off offset:2048
	global_load_dwordx4 v[62:65], v[42:43], off
	global_load_dword v47, v[44:45], off offset:4
	global_load_dword v55, v[44:45], off offset:2052
	global_load_dwordx4 v[66:69], v[42:43], off offset:512
	global_load_dword v48, v[44:45], off offset:8
	global_load_dword v56, v[44:45], off offset:2056
	global_load_dwordx4 v[70:73], v[42:43], off offset:1024
	global_load_dword v49, v[44:45], off offset:12
	global_load_dword v57, v[44:45], off offset:2060
	global_load_dwordx4 v[74:77], v[42:43], off offset:1536
	global_load_dword v50, v[44:45], off offset:16
	global_load_dword v58, v[44:45], off offset:2064
	global_load_dwordx4 v[78:81], v[42:43], off offset:2048
	global_load_dword v51, v[44:45], off offset:20
	global_load_dword v59, v[44:45], off offset:2068
	global_load_dwordx4 v[82:85], v[42:43], off offset:2560
	global_load_dword v52, v[44:45], off offset:24
	global_load_dword v60, v[44:45], off offset:2072
	global_load_dwordx4 v[86:89], v[42:43], off offset:3072
	global_load_dword v53, v[44:45], off offset:28
	global_load_dword v61, v[44:45], off offset:2076
	global_load_dwordx4 v[90:93], v[42:43], off offset:3584
	v_lshl_add_u64 v[42:43], v[42:43], 0, s[6:7]
	v_lshl_add_u64 v[42:43], v[42:43], 0, s[6:7]
	global_load_dword v94, v[44:45], off offset:32
	global_load_dword v102, v[44:45], off offset:2080
	global_load_dwordx4 v[110:113], v[42:43], off
	global_load_dword v95, v[44:45], off offset:36
	global_load_dword v103, v[44:45], off offset:2084
	global_load_dwordx4 v[114:117], v[42:43], off offset:512
	global_load_dword v96, v[44:45], off offset:40
	global_load_dword v104, v[44:45], off offset:2088
	global_load_dwordx4 v[118:121], v[42:43], off offset:1024
	global_load_dword v97, v[44:45], off offset:44
	global_load_dword v105, v[44:45], off offset:2092
	global_load_dwordx4 v[122:125], v[42:43], off offset:1536
	global_load_dword v98, v[44:45], off offset:48
	global_load_dword v106, v[44:45], off offset:2096
	global_load_dwordx4 v[126:129], v[42:43], off offset:2048
	global_load_dword v99, v[44:45], off offset:52
	global_load_dword v107, v[44:45], off offset:2100
	global_load_dwordx4 v[130:133], v[42:43], off offset:2560
	global_load_dword v100, v[44:45], off offset:56
	global_load_dword v108, v[44:45], off offset:2104
	global_load_dwordx4 v[134:137], v[42:43], off offset:3072
	global_load_dword v101, v[44:45], off offset:60
	global_load_dword v109, v[44:45], off offset:2108
	global_load_dwordx4 v[138:141], v[42:43], off offset:3584
	v_lshl_add_u64 v[42:43], v[42:43], 0, s[6:7]
	v_lshl_add_u64 v[42:43], v[42:43], 0, s[6:7]
	s_waitcnt vmcnt(24)
	global_store_dwordx4 v[40:41], v[2:5], off
	v_add_f32_e32 v1, v1, v46
	v_max_f32_e32 v20, v54, v54
	v_max_f32_e32 v23, v1, v20
	v_sub_f32_e32 v20, v54, v23
	v_sub_f32_e32 v1, v1, v23
	v_mul_f32_e32 v20, 0x3fb8aa3b, v20
	v_mul_f32_e32 v1, 0x3fb8aa3b, v1
	v_exp_f32_e32 v20, v20
	v_exp_f32_e32 v22, v1
	s_nop 0
	v_pk_mul_f32 v[64:65], v[64:65], v[20:21] op_sel_hi:[1,0]
	v_pk_mul_f32 v[62:63], v[62:63], v[20:21] op_sel_hi:[1,0]
	v_pk_fma_f32 v[4:5], v[4:5], v[22:23], v[64:65] op_sel_hi:[1,0,1]
	v_pk_fma_f32 v[2:3], v[2:3], v[22:23], v[62:63] op_sel_hi:[1,0,1]
	v_mov_b32_e32 v1, v23
	global_store_dwordx4 v[40:41], v[2:5], off offset:512
	v_add_f32_e32 v1, v1, v47
	v_max_f32_e32 v20, v55, v55
	v_max_f32_e32 v23, v1, v20
	v_sub_f32_e32 v20, v55, v23
	v_sub_f32_e32 v1, v1, v23
	v_mul_f32_e32 v20, 0x3fb8aa3b, v20
	v_mul_f32_e32 v1, 0x3fb8aa3b, v1
	v_exp_f32_e32 v20, v20
	v_exp_f32_e32 v22, v1
	s_nop 0
	v_pk_mul_f32 v[68:69], v[68:69], v[20:21] op_sel_hi:[1,0]
	v_pk_mul_f32 v[66:67], v[66:67], v[20:21] op_sel_hi:[1,0]
	v_pk_fma_f32 v[4:5], v[4:5], v[22:23], v[68:69] op_sel_hi:[1,0,1]
	v_pk_fma_f32 v[2:3], v[2:3], v[22:23], v[66:67] op_sel_hi:[1,0,1]
	v_mov_b32_e32 v1, v23
	global_store_dwordx4 v[40:41], v[2:5], off offset:1024
	v_add_f32_e32 v1, v1, v48
	v_max_f32_e32 v20, v56, v56
	v_max_f32_e32 v23, v1, v20
	v_sub_f32_e32 v20, v56, v23
	v_sub_f32_e32 v1, v1, v23
	v_mul_f32_e32 v20, 0x3fb8aa3b, v20
	v_mul_f32_e32 v1, 0x3fb8aa3b, v1
	v_exp_f32_e32 v20, v20
	v_exp_f32_e32 v22, v1
	s_nop 0
	v_pk_mul_f32 v[72:73], v[72:73], v[20:21] op_sel_hi:[1,0]
	v_pk_mul_f32 v[70:71], v[70:71], v[20:21] op_sel_hi:[1,0]
	v_pk_fma_f32 v[4:5], v[4:5], v[22:23], v[72:73] op_sel_hi:[1,0,1]
	v_pk_fma_f32 v[2:3], v[2:3], v[22:23], v[70:71] op_sel_hi:[1,0,1]
	v_mov_b32_e32 v1, v23
	global_store_dwordx4 v[40:41], v[2:5], off offset:1536
	v_add_f32_e32 v1, v1, v49
	v_max_f32_e32 v20, v57, v57
	v_max_f32_e32 v23, v1, v20
	v_sub_f32_e32 v20, v57, v23
	v_sub_f32_e32 v1, v1, v23
	v_mul_f32_e32 v20, 0x3fb8aa3b, v20
	v_mul_f32_e32 v1, 0x3fb8aa3b, v1
	v_exp_f32_e32 v20, v20
	v_exp_f32_e32 v22, v1
	s_nop 0
	v_pk_mul_f32 v[76:77], v[76:77], v[20:21] op_sel_hi:[1,0]
	v_pk_mul_f32 v[74:75], v[74:75], v[20:21] op_sel_hi:[1,0]
	v_pk_fma_f32 v[4:5], v[4:5], v[22:23], v[76:77] op_sel_hi:[1,0,1]
	v_pk_fma_f32 v[2:3], v[2:3], v[22:23], v[74:75] op_sel_hi:[1,0,1]
	v_mov_b32_e32 v1, v23
	global_store_dwordx4 v[40:41], v[2:5], off offset:2048
	v_add_f32_e32 v1, v1, v50
	v_max_f32_e32 v20, v58, v58
	v_max_f32_e32 v23, v1, v20
	v_sub_f32_e32 v20, v58, v23
	v_sub_f32_e32 v1, v1, v23
	v_mul_f32_e32 v20, 0x3fb8aa3b, v20
	v_mul_f32_e32 v1, 0x3fb8aa3b, v1
	v_exp_f32_e32 v20, v20
	v_exp_f32_e32 v22, v1
	s_nop 0
	v_pk_mul_f32 v[80:81], v[80:81], v[20:21] op_sel_hi:[1,0]
	v_pk_mul_f32 v[78:79], v[78:79], v[20:21] op_sel_hi:[1,0]
	v_pk_fma_f32 v[4:5], v[4:5], v[22:23], v[80:81] op_sel_hi:[1,0,1]
	v_pk_fma_f32 v[2:3], v[2:3], v[22:23], v[78:79] op_sel_hi:[1,0,1]
	v_mov_b32_e32 v1, v23
	global_store_dwordx4 v[40:41], v[2:5], off offset:2560
	v_add_f32_e32 v1, v1, v51
	v_max_f32_e32 v20, v59, v59
	v_max_f32_e32 v23, v1, v20
	v_sub_f32_e32 v20, v59, v23
	v_sub_f32_e32 v1, v1, v23
	v_mul_f32_e32 v20, 0x3fb8aa3b, v20
	v_mul_f32_e32 v1, 0x3fb8aa3b, v1
	v_exp_f32_e32 v20, v20
	v_exp_f32_e32 v22, v1
	s_nop 0
	v_pk_mul_f32 v[84:85], v[84:85], v[20:21] op_sel_hi:[1,0]
	v_pk_mul_f32 v[82:83], v[82:83], v[20:21] op_sel_hi:[1,0]
	v_pk_fma_f32 v[4:5], v[4:5], v[22:23], v[84:85] op_sel_hi:[1,0,1]
	v_pk_fma_f32 v[2:3], v[2:3], v[22:23], v[82:83] op_sel_hi:[1,0,1]
	v_mov_b32_e32 v1, v23
	global_store_dwordx4 v[40:41], v[2:5], off offset:3072
	v_add_f32_e32 v1, v1, v52
	v_max_f32_e32 v20, v60, v60
	v_max_f32_e32 v23, v1, v20
	v_sub_f32_e32 v20, v60, v23
	v_sub_f32_e32 v1, v1, v23
	v_mul_f32_e32 v20, 0x3fb8aa3b, v20
	v_mul_f32_e32 v1, 0x3fb8aa3b, v1
	v_exp_f32_e32 v20, v20
	v_exp_f32_e32 v22, v1
	s_nop 0
	v_pk_mul_f32 v[88:89], v[88:89], v[20:21] op_sel_hi:[1,0]
	v_pk_mul_f32 v[86:87], v[86:87], v[20:21] op_sel_hi:[1,0]
	v_pk_fma_f32 v[4:5], v[4:5], v[22:23], v[88:89] op_sel_hi:[1,0,1]
	v_pk_fma_f32 v[2:3], v[2:3], v[22:23], v[86:87] op_sel_hi:[1,0,1]
	v_mov_b32_e32 v1, v23
	global_store_dwordx4 v[40:41], v[2:5], off offset:3584
	v_add_f32_e32 v1, v1, v53
	v_max_f32_e32 v20, v61, v61
	v_max_f32_e32 v23, v1, v20
	v_sub_f32_e32 v20, v61, v23
	v_sub_f32_e32 v1, v1, v23
	v_mul_f32_e32 v20, 0x3fb8aa3b, v20
	v_mul_f32_e32 v1, 0x3fb8aa3b, v1
	v_exp_f32_e32 v20, v20
	v_exp_f32_e32 v22, v1
	s_nop 0
	v_pk_mul_f32 v[92:93], v[92:93], v[20:21] op_sel_hi:[1,0]
	v_pk_mul_f32 v[90:91], v[90:91], v[20:21] op_sel_hi:[1,0]
	v_pk_fma_f32 v[4:5], v[4:5], v[22:23], v[92:93] op_sel_hi:[1,0,1]
	v_pk_fma_f32 v[2:3], v[2:3], v[22:23], v[90:91] op_sel_hi:[1,0,1]
	v_mov_b32_e32 v1, v23
	v_lshl_add_u64 v[40:41], v[40:41], 0, s[6:7]
	v_lshl_add_u64 v[40:41], v[40:41], 0, s[6:7]
	global_load_dword v46, v[44:45], off offset:64
	global_load_dword v54, v[44:45], off offset:2112
	global_load_dwordx4 v[62:65], v[42:43], off
	global_load_dword v47, v[44:45], off offset:68
	global_load_dword v55, v[44:45], off offset:2116
	global_load_dwordx4 v[66:69], v[42:43], off offset:512
	global_load_dword v48, v[44:45], off offset:72
	global_load_dword v56, v[44:45], off offset:2120
	global_load_dwordx4 v[70:73], v[42:43], off offset:1024
	global_load_dword v49, v[44:45], off offset:76
	global_load_dword v57, v[44:45], off offset:2124
	global_load_dwordx4 v[74:77], v[42:43], off offset:1536
	global_load_dword v50, v[44:45], off offset:80
	global_load_dword v58, v[44:45], off offset:2128
	global_load_dwordx4 v[78:81], v[42:43], off offset:2048
	global_load_dword v51, v[44:45], off offset:84
	global_load_dword v59, v[44:45], off offset:2132
	global_load_dwordx4 v[82:85], v[42:43], off offset:2560
	global_load_dword v52, v[44:45], off offset:88
	global_load_dword v60, v[44:45], off offset:2136
	global_load_dwordx4 v[86:89], v[42:43], off offset:3072
	global_load_dword v53, v[44:45], off offset:92
	global_load_dword v61, v[44:45], off offset:2140
	global_load_dwordx4 v[90:93], v[42:43], off offset:3584
	v_lshl_add_u64 v[42:43], v[42:43], 0, s[6:7]
	v_lshl_add_u64 v[42:43], v[42:43], 0, s[6:7]
	s_waitcnt vmcnt(32)
	global_store_dwordx4 v[40:41], v[2:5], off
	v_add_f32_e32 v1, v1, v94
	v_max_f32_e32 v20, v102, v102
	v_max_f32_e32 v23, v1, v20
	v_sub_f32_e32 v20, v102, v23
	v_sub_f32_e32 v1, v1, v23
	v_mul_f32_e32 v20, 0x3fb8aa3b, v20
	v_mul_f32_e32 v1, 0x3fb8aa3b, v1
	v_exp_f32_e32 v20, v20
	v_exp_f32_e32 v22, v1
	s_nop 0
	v_pk_mul_f32 v[112:113], v[112:113], v[20:21] op_sel_hi:[1,0]
	v_pk_mul_f32 v[110:111], v[110:111], v[20:21] op_sel_hi:[1,0]
	v_pk_fma_f32 v[4:5], v[4:5], v[22:23], v[112:113] op_sel_hi:[1,0,1]
	v_pk_fma_f32 v[2:3], v[2:3], v[22:23], v[110:111] op_sel_hi:[1,0,1]
	v_mov_b32_e32 v1, v23
	global_store_dwordx4 v[40:41], v[2:5], off offset:512
	v_add_f32_e32 v1, v1, v95
	v_max_f32_e32 v20, v103, v103
	v_max_f32_e32 v23, v1, v20
	v_sub_f32_e32 v20, v103, v23
	v_sub_f32_e32 v1, v1, v23
	v_mul_f32_e32 v20, 0x3fb8aa3b, v20
	v_mul_f32_e32 v1, 0x3fb8aa3b, v1
	v_exp_f32_e32 v20, v20
	v_exp_f32_e32 v22, v1
	s_nop 0
	v_pk_mul_f32 v[116:117], v[116:117], v[20:21] op_sel_hi:[1,0]
	v_pk_mul_f32 v[114:115], v[114:115], v[20:21] op_sel_hi:[1,0]
	v_pk_fma_f32 v[4:5], v[4:5], v[22:23], v[116:117] op_sel_hi:[1,0,1]
	v_pk_fma_f32 v[2:3], v[2:3], v[22:23], v[114:115] op_sel_hi:[1,0,1]
	v_mov_b32_e32 v1, v23
	global_store_dwordx4 v[40:41], v[2:5], off offset:1024
	v_add_f32_e32 v1, v1, v96
	v_max_f32_e32 v20, v104, v104
	v_max_f32_e32 v23, v1, v20
	v_sub_f32_e32 v20, v104, v23
	v_sub_f32_e32 v1, v1, v23
	v_mul_f32_e32 v20, 0x3fb8aa3b, v20
	v_mul_f32_e32 v1, 0x3fb8aa3b, v1
	v_exp_f32_e32 v20, v20
	v_exp_f32_e32 v22, v1
	s_nop 0
	v_pk_mul_f32 v[120:121], v[120:121], v[20:21] op_sel_hi:[1,0]
	v_pk_mul_f32 v[118:119], v[118:119], v[20:21] op_sel_hi:[1,0]
	v_pk_fma_f32 v[4:5], v[4:5], v[22:23], v[120:121] op_sel_hi:[1,0,1]
	v_pk_fma_f32 v[2:3], v[2:3], v[22:23], v[118:119] op_sel_hi:[1,0,1]
	v_mov_b32_e32 v1, v23
	global_store_dwordx4 v[40:41], v[2:5], off offset:1536
	v_add_f32_e32 v1, v1, v97
	v_max_f32_e32 v20, v105, v105
	v_max_f32_e32 v23, v1, v20
	v_sub_f32_e32 v20, v105, v23
	v_sub_f32_e32 v1, v1, v23
	v_mul_f32_e32 v20, 0x3fb8aa3b, v20
	v_mul_f32_e32 v1, 0x3fb8aa3b, v1
	v_exp_f32_e32 v20, v20
	v_exp_f32_e32 v22, v1
	s_nop 0
	v_pk_mul_f32 v[124:125], v[124:125], v[20:21] op_sel_hi:[1,0]
	v_pk_mul_f32 v[122:123], v[122:123], v[20:21] op_sel_hi:[1,0]
	v_pk_fma_f32 v[4:5], v[4:5], v[22:23], v[124:125] op_sel_hi:[1,0,1]
	v_pk_fma_f32 v[2:3], v[2:3], v[22:23], v[122:123] op_sel_hi:[1,0,1]
	v_mov_b32_e32 v1, v23
	global_store_dwordx4 v[40:41], v[2:5], off offset:2048
	v_add_f32_e32 v1, v1, v98
	v_max_f32_e32 v20, v106, v106
	v_max_f32_e32 v23, v1, v20
	v_sub_f32_e32 v20, v106, v23
	v_sub_f32_e32 v1, v1, v23
	v_mul_f32_e32 v20, 0x3fb8aa3b, v20
	v_mul_f32_e32 v1, 0x3fb8aa3b, v1
	v_exp_f32_e32 v20, v20
	v_exp_f32_e32 v22, v1
	s_nop 0
	v_pk_mul_f32 v[128:129], v[128:129], v[20:21] op_sel_hi:[1,0]
	v_pk_mul_f32 v[126:127], v[126:127], v[20:21] op_sel_hi:[1,0]
	v_pk_fma_f32 v[4:5], v[4:5], v[22:23], v[128:129] op_sel_hi:[1,0,1]
	v_pk_fma_f32 v[2:3], v[2:3], v[22:23], v[126:127] op_sel_hi:[1,0,1]
	v_mov_b32_e32 v1, v23
	global_store_dwordx4 v[40:41], v[2:5], off offset:2560
	v_add_f32_e32 v1, v1, v99
	v_max_f32_e32 v20, v107, v107
	v_max_f32_e32 v23, v1, v20
	v_sub_f32_e32 v20, v107, v23
	v_sub_f32_e32 v1, v1, v23
	v_mul_f32_e32 v20, 0x3fb8aa3b, v20
	v_mul_f32_e32 v1, 0x3fb8aa3b, v1
	v_exp_f32_e32 v20, v20
	v_exp_f32_e32 v22, v1
	s_nop 0
	v_pk_mul_f32 v[132:133], v[132:133], v[20:21] op_sel_hi:[1,0]
	v_pk_mul_f32 v[130:131], v[130:131], v[20:21] op_sel_hi:[1,0]
	v_pk_fma_f32 v[4:5], v[4:5], v[22:23], v[132:133] op_sel_hi:[1,0,1]
	v_pk_fma_f32 v[2:3], v[2:3], v[22:23], v[130:131] op_sel_hi:[1,0,1]
	v_mov_b32_e32 v1, v23
	global_store_dwordx4 v[40:41], v[2:5], off offset:3072
	v_add_f32_e32 v1, v1, v100
	v_max_f32_e32 v20, v108, v108
	v_max_f32_e32 v23, v1, v20
	v_sub_f32_e32 v20, v108, v23
	v_sub_f32_e32 v1, v1, v23
	v_mul_f32_e32 v20, 0x3fb8aa3b, v20
	v_mul_f32_e32 v1, 0x3fb8aa3b, v1
	v_exp_f32_e32 v20, v20
	v_exp_f32_e32 v22, v1
	s_nop 0
	v_pk_mul_f32 v[136:137], v[136:137], v[20:21] op_sel_hi:[1,0]
	v_pk_mul_f32 v[134:135], v[134:135], v[20:21] op_sel_hi:[1,0]
	v_pk_fma_f32 v[4:5], v[4:5], v[22:23], v[136:137] op_sel_hi:[1,0,1]
	v_pk_fma_f32 v[2:3], v[2:3], v[22:23], v[134:135] op_sel_hi:[1,0,1]
	v_mov_b32_e32 v1, v23
	global_store_dwordx4 v[40:41], v[2:5], off offset:3584
	v_add_f32_e32 v1, v1, v101
	v_max_f32_e32 v20, v109, v109
	v_max_f32_e32 v23, v1, v20
	v_sub_f32_e32 v20, v109, v23
	v_sub_f32_e32 v1, v1, v23
	v_mul_f32_e32 v20, 0x3fb8aa3b, v20
	v_mul_f32_e32 v1, 0x3fb8aa3b, v1
	v_exp_f32_e32 v20, v20
	v_exp_f32_e32 v22, v1
	s_nop 0
	v_pk_mul_f32 v[140:141], v[140:141], v[20:21] op_sel_hi:[1,0]
	v_pk_mul_f32 v[138:139], v[138:139], v[20:21] op_sel_hi:[1,0]
	v_pk_fma_f32 v[4:5], v[4:5], v[22:23], v[140:141] op_sel_hi:[1,0,1]
	v_pk_fma_f32 v[2:3], v[2:3], v[22:23], v[138:139] op_sel_hi:[1,0,1]
	v_mov_b32_e32 v1, v23
	v_lshl_add_u64 v[40:41], v[40:41], 0, s[6:7]
	v_lshl_add_u64 v[40:41], v[40:41], 0, s[6:7]
	global_load_dword v94, v[44:45], off offset:96
	global_load_dword v102, v[44:45], off offset:2144
	global_load_dwordx4 v[110:113], v[42:43], off
	global_load_dword v95, v[44:45], off offset:100
	global_load_dword v103, v[44:45], off offset:2148
	global_load_dwordx4 v[114:117], v[42:43], off offset:512
	global_load_dword v96, v[44:45], off offset:104
	global_load_dword v104, v[44:45], off offset:2152
	global_load_dwordx4 v[118:121], v[42:43], off offset:1024
	global_load_dword v97, v[44:45], off offset:108
	global_load_dword v105, v[44:45], off offset:2156
	global_load_dwordx4 v[122:125], v[42:43], off offset:1536
	global_load_dword v98, v[44:45], off offset:112
	global_load_dword v106, v[44:45], off offset:2160
	global_load_dwordx4 v[126:129], v[42:43], off offset:2048
	global_load_dword v99, v[44:45], off offset:116
	global_load_dword v107, v[44:45], off offset:2164
	global_load_dwordx4 v[130:133], v[42:43], off offset:2560
	global_load_dword v100, v[44:45], off offset:120
	global_load_dword v108, v[44:45], off offset:2168
	global_load_dwordx4 v[134:137], v[42:43], off offset:3072
	global_load_dword v101, v[44:45], off offset:124
	global_load_dword v109, v[44:45], off offset:2172
	global_load_dwordx4 v[138:141], v[42:43], off offset:3584
	v_lshl_add_u64 v[42:43], v[42:43], 0, s[6:7]
	v_lshl_add_u64 v[42:43], v[42:43], 0, s[6:7]
	s_waitcnt vmcnt(32)
	global_store_dwordx4 v[40:41], v[2:5], off
	v_add_f32_e32 v1, v1, v46
	v_max_f32_e32 v20, v54, v54
	v_max_f32_e32 v23, v1, v20
	v_sub_f32_e32 v20, v54, v23
	v_sub_f32_e32 v1, v1, v23
	v_mul_f32_e32 v20, 0x3fb8aa3b, v20
	v_mul_f32_e32 v1, 0x3fb8aa3b, v1
	v_exp_f32_e32 v20, v20
	v_exp_f32_e32 v22, v1
	s_nop 0
	v_pk_mul_f32 v[64:65], v[64:65], v[20:21] op_sel_hi:[1,0]
	v_pk_mul_f32 v[62:63], v[62:63], v[20:21] op_sel_hi:[1,0]
	v_pk_fma_f32 v[4:5], v[4:5], v[22:23], v[64:65] op_sel_hi:[1,0,1]
	v_pk_fma_f32 v[2:3], v[2:3], v[22:23], v[62:63] op_sel_hi:[1,0,1]
	v_mov_b32_e32 v1, v23
	global_store_dwordx4 v[40:41], v[2:5], off offset:512
	v_add_f32_e32 v1, v1, v47
	v_max_f32_e32 v20, v55, v55
	v_max_f32_e32 v23, v1, v20
	v_sub_f32_e32 v20, v55, v23
	v_sub_f32_e32 v1, v1, v23
	v_mul_f32_e32 v20, 0x3fb8aa3b, v20
	v_mul_f32_e32 v1, 0x3fb8aa3b, v1
	v_exp_f32_e32 v20, v20
	v_exp_f32_e32 v22, v1
	s_nop 0
	v_pk_mul_f32 v[68:69], v[68:69], v[20:21] op_sel_hi:[1,0]
	v_pk_mul_f32 v[66:67], v[66:67], v[20:21] op_sel_hi:[1,0]
	v_pk_fma_f32 v[4:5], v[4:5], v[22:23], v[68:69] op_sel_hi:[1,0,1]
	v_pk_fma_f32 v[2:3], v[2:3], v[22:23], v[66:67] op_sel_hi:[1,0,1]
	v_mov_b32_e32 v1, v23
	global_store_dwordx4 v[40:41], v[2:5], off offset:1024
	v_add_f32_e32 v1, v1, v48
	v_max_f32_e32 v20, v56, v56
	v_max_f32_e32 v23, v1, v20
	v_sub_f32_e32 v20, v56, v23
	v_sub_f32_e32 v1, v1, v23
	v_mul_f32_e32 v20, 0x3fb8aa3b, v20
	v_mul_f32_e32 v1, 0x3fb8aa3b, v1
	v_exp_f32_e32 v20, v20
	v_exp_f32_e32 v22, v1
	s_nop 0
	v_pk_mul_f32 v[72:73], v[72:73], v[20:21] op_sel_hi:[1,0]
	v_pk_mul_f32 v[70:71], v[70:71], v[20:21] op_sel_hi:[1,0]
	v_pk_fma_f32 v[4:5], v[4:5], v[22:23], v[72:73] op_sel_hi:[1,0,1]
	v_pk_fma_f32 v[2:3], v[2:3], v[22:23], v[70:71] op_sel_hi:[1,0,1]
	v_mov_b32_e32 v1, v23
	global_store_dwordx4 v[40:41], v[2:5], off offset:1536
	v_add_f32_e32 v1, v1, v49
	v_max_f32_e32 v20, v57, v57
	v_max_f32_e32 v23, v1, v20
	v_sub_f32_e32 v20, v57, v23
	v_sub_f32_e32 v1, v1, v23
	v_mul_f32_e32 v20, 0x3fb8aa3b, v20
	v_mul_f32_e32 v1, 0x3fb8aa3b, v1
	v_exp_f32_e32 v20, v20
	v_exp_f32_e32 v22, v1
	s_nop 0
	v_pk_mul_f32 v[76:77], v[76:77], v[20:21] op_sel_hi:[1,0]
	v_pk_mul_f32 v[74:75], v[74:75], v[20:21] op_sel_hi:[1,0]
	v_pk_fma_f32 v[4:5], v[4:5], v[22:23], v[76:77] op_sel_hi:[1,0,1]
	v_pk_fma_f32 v[2:3], v[2:3], v[22:23], v[74:75] op_sel_hi:[1,0,1]
	v_mov_b32_e32 v1, v23
	global_store_dwordx4 v[40:41], v[2:5], off offset:2048
	v_add_f32_e32 v1, v1, v50
	v_max_f32_e32 v20, v58, v58
	v_max_f32_e32 v23, v1, v20
	v_sub_f32_e32 v20, v58, v23
	v_sub_f32_e32 v1, v1, v23
	v_mul_f32_e32 v20, 0x3fb8aa3b, v20
	v_mul_f32_e32 v1, 0x3fb8aa3b, v1
	v_exp_f32_e32 v20, v20
	v_exp_f32_e32 v22, v1
	s_nop 0
	v_pk_mul_f32 v[80:81], v[80:81], v[20:21] op_sel_hi:[1,0]
	v_pk_mul_f32 v[78:79], v[78:79], v[20:21] op_sel_hi:[1,0]
	v_pk_fma_f32 v[4:5], v[4:5], v[22:23], v[80:81] op_sel_hi:[1,0,1]
	v_pk_fma_f32 v[2:3], v[2:3], v[22:23], v[78:79] op_sel_hi:[1,0,1]
	v_mov_b32_e32 v1, v23
	global_store_dwordx4 v[40:41], v[2:5], off offset:2560
	v_add_f32_e32 v1, v1, v51
	v_max_f32_e32 v20, v59, v59
	v_max_f32_e32 v23, v1, v20
	v_sub_f32_e32 v20, v59, v23
	v_sub_f32_e32 v1, v1, v23
	v_mul_f32_e32 v20, 0x3fb8aa3b, v20
	v_mul_f32_e32 v1, 0x3fb8aa3b, v1
	v_exp_f32_e32 v20, v20
	v_exp_f32_e32 v22, v1
	s_nop 0
	v_pk_mul_f32 v[84:85], v[84:85], v[20:21] op_sel_hi:[1,0]
	v_pk_mul_f32 v[82:83], v[82:83], v[20:21] op_sel_hi:[1,0]
	v_pk_fma_f32 v[4:5], v[4:5], v[22:23], v[84:85] op_sel_hi:[1,0,1]
	v_pk_fma_f32 v[2:3], v[2:3], v[22:23], v[82:83] op_sel_hi:[1,0,1]
	v_mov_b32_e32 v1, v23
	global_store_dwordx4 v[40:41], v[2:5], off offset:3072
	v_add_f32_e32 v1, v1, v52
	v_max_f32_e32 v20, v60, v60
	v_max_f32_e32 v23, v1, v20
	v_sub_f32_e32 v20, v60, v23
	v_sub_f32_e32 v1, v1, v23
	v_mul_f32_e32 v20, 0x3fb8aa3b, v20
	v_mul_f32_e32 v1, 0x3fb8aa3b, v1
	v_exp_f32_e32 v20, v20
	v_exp_f32_e32 v22, v1
	s_nop 0
	v_pk_mul_f32 v[88:89], v[88:89], v[20:21] op_sel_hi:[1,0]
	v_pk_mul_f32 v[86:87], v[86:87], v[20:21] op_sel_hi:[1,0]
	v_pk_fma_f32 v[4:5], v[4:5], v[22:23], v[88:89] op_sel_hi:[1,0,1]
	v_pk_fma_f32 v[2:3], v[2:3], v[22:23], v[86:87] op_sel_hi:[1,0,1]
	v_mov_b32_e32 v1, v23
	global_store_dwordx4 v[40:41], v[2:5], off offset:3584
	v_add_f32_e32 v1, v1, v53
	v_max_f32_e32 v20, v61, v61
	v_max_f32_e32 v23, v1, v20
	v_sub_f32_e32 v20, v61, v23
	v_sub_f32_e32 v1, v1, v23
	v_mul_f32_e32 v20, 0x3fb8aa3b, v20
	v_mul_f32_e32 v1, 0x3fb8aa3b, v1
	v_exp_f32_e32 v20, v20
	v_exp_f32_e32 v22, v1
	s_nop 0
	v_pk_mul_f32 v[92:93], v[92:93], v[20:21] op_sel_hi:[1,0]
	v_pk_mul_f32 v[90:91], v[90:91], v[20:21] op_sel_hi:[1,0]
	v_pk_fma_f32 v[4:5], v[4:5], v[22:23], v[92:93] op_sel_hi:[1,0,1]
	v_pk_fma_f32 v[2:3], v[2:3], v[22:23], v[90:91] op_sel_hi:[1,0,1]
	v_mov_b32_e32 v1, v23
	v_lshl_add_u64 v[40:41], v[40:41], 0, s[6:7]
	v_lshl_add_u64 v[40:41], v[40:41], 0, s[6:7]
	s_waitcnt vmcnt(8)
	global_store_dwordx4 v[40:41], v[2:5], off
	v_add_f32_e32 v1, v1, v94
	v_max_f32_e32 v20, v102, v102
	v_max_f32_e32 v23, v1, v20
	v_sub_f32_e32 v20, v102, v23
	v_sub_f32_e32 v1, v1, v23
	v_mul_f32_e32 v20, 0x3fb8aa3b, v20
	v_mul_f32_e32 v1, 0x3fb8aa3b, v1
	v_exp_f32_e32 v20, v20
	v_exp_f32_e32 v22, v1
	s_nop 0
	v_pk_mul_f32 v[112:113], v[112:113], v[20:21] op_sel_hi:[1,0]
	v_pk_mul_f32 v[110:111], v[110:111], v[20:21] op_sel_hi:[1,0]
	v_pk_fma_f32 v[4:5], v[4:5], v[22:23], v[112:113] op_sel_hi:[1,0,1]
	v_pk_fma_f32 v[2:3], v[2:3], v[22:23], v[110:111] op_sel_hi:[1,0,1]
	v_mov_b32_e32 v1, v23
	global_store_dwordx4 v[40:41], v[2:5], off offset:512
	v_add_f32_e32 v1, v1, v95
	v_max_f32_e32 v20, v103, v103
	v_max_f32_e32 v23, v1, v20
	v_sub_f32_e32 v20, v103, v23
	v_sub_f32_e32 v1, v1, v23
	v_mul_f32_e32 v20, 0x3fb8aa3b, v20
	v_mul_f32_e32 v1, 0x3fb8aa3b, v1
	v_exp_f32_e32 v20, v20
	v_exp_f32_e32 v22, v1
	s_nop 0
	v_pk_mul_f32 v[116:117], v[116:117], v[20:21] op_sel_hi:[1,0]
	v_pk_mul_f32 v[114:115], v[114:115], v[20:21] op_sel_hi:[1,0]
	v_pk_fma_f32 v[4:5], v[4:5], v[22:23], v[116:117] op_sel_hi:[1,0,1]
	v_pk_fma_f32 v[2:3], v[2:3], v[22:23], v[114:115] op_sel_hi:[1,0,1]
	v_mov_b32_e32 v1, v23
	global_store_dwordx4 v[40:41], v[2:5], off offset:1024
	v_add_f32_e32 v1, v1, v96
	v_max_f32_e32 v20, v104, v104
	v_max_f32_e32 v23, v1, v20
	v_sub_f32_e32 v20, v104, v23
	v_sub_f32_e32 v1, v1, v23
	v_mul_f32_e32 v20, 0x3fb8aa3b, v20
	v_mul_f32_e32 v1, 0x3fb8aa3b, v1
	v_exp_f32_e32 v20, v20
	v_exp_f32_e32 v22, v1
	s_nop 0
	v_pk_mul_f32 v[120:121], v[120:121], v[20:21] op_sel_hi:[1,0]
	v_pk_mul_f32 v[118:119], v[118:119], v[20:21] op_sel_hi:[1,0]
	v_pk_fma_f32 v[4:5], v[4:5], v[22:23], v[120:121] op_sel_hi:[1,0,1]
	v_pk_fma_f32 v[2:3], v[2:3], v[22:23], v[118:119] op_sel_hi:[1,0,1]
	v_mov_b32_e32 v1, v23
	global_store_dwordx4 v[40:41], v[2:5], off offset:1536
	v_add_f32_e32 v1, v1, v97
	v_max_f32_e32 v20, v105, v105
	v_max_f32_e32 v23, v1, v20
	v_sub_f32_e32 v20, v105, v23
	v_sub_f32_e32 v1, v1, v23
	v_mul_f32_e32 v20, 0x3fb8aa3b, v20
	v_mul_f32_e32 v1, 0x3fb8aa3b, v1
	v_exp_f32_e32 v20, v20
	v_exp_f32_e32 v22, v1
	s_nop 0
	v_pk_mul_f32 v[124:125], v[124:125], v[20:21] op_sel_hi:[1,0]
	v_pk_mul_f32 v[122:123], v[122:123], v[20:21] op_sel_hi:[1,0]
	v_pk_fma_f32 v[4:5], v[4:5], v[22:23], v[124:125] op_sel_hi:[1,0,1]
	v_pk_fma_f32 v[2:3], v[2:3], v[22:23], v[122:123] op_sel_hi:[1,0,1]
	v_mov_b32_e32 v1, v23
	global_store_dwordx4 v[40:41], v[2:5], off offset:2048
	v_add_f32_e32 v1, v1, v98
	v_max_f32_e32 v20, v106, v106
	v_max_f32_e32 v23, v1, v20
	v_sub_f32_e32 v20, v106, v23
	v_sub_f32_e32 v1, v1, v23
	v_mul_f32_e32 v20, 0x3fb8aa3b, v20
	v_mul_f32_e32 v1, 0x3fb8aa3b, v1
	v_exp_f32_e32 v20, v20
	v_exp_f32_e32 v22, v1
	s_nop 0
	v_pk_mul_f32 v[128:129], v[128:129], v[20:21] op_sel_hi:[1,0]
	v_pk_mul_f32 v[126:127], v[126:127], v[20:21] op_sel_hi:[1,0]
	v_pk_fma_f32 v[4:5], v[4:5], v[22:23], v[128:129] op_sel_hi:[1,0,1]
	v_pk_fma_f32 v[2:3], v[2:3], v[22:23], v[126:127] op_sel_hi:[1,0,1]
	v_mov_b32_e32 v1, v23
	global_store_dwordx4 v[40:41], v[2:5], off offset:2560
	v_add_f32_e32 v1, v1, v99
	v_max_f32_e32 v20, v107, v107
	v_max_f32_e32 v23, v1, v20
	v_sub_f32_e32 v20, v107, v23
	v_sub_f32_e32 v1, v1, v23
	v_mul_f32_e32 v20, 0x3fb8aa3b, v20
	v_mul_f32_e32 v1, 0x3fb8aa3b, v1
	v_exp_f32_e32 v20, v20
	v_exp_f32_e32 v22, v1
	s_nop 0
	v_pk_mul_f32 v[132:133], v[132:133], v[20:21] op_sel_hi:[1,0]
	v_pk_mul_f32 v[130:131], v[130:131], v[20:21] op_sel_hi:[1,0]
	v_pk_fma_f32 v[4:5], v[4:5], v[22:23], v[132:133] op_sel_hi:[1,0,1]
	v_pk_fma_f32 v[2:3], v[2:3], v[22:23], v[130:131] op_sel_hi:[1,0,1]
	v_mov_b32_e32 v1, v23
	global_store_dwordx4 v[40:41], v[2:5], off offset:3072
	v_add_f32_e32 v1, v1, v100
	v_max_f32_e32 v20, v108, v108
	v_max_f32_e32 v23, v1, v20
	v_sub_f32_e32 v20, v108, v23
	v_sub_f32_e32 v1, v1, v23
	v_mul_f32_e32 v20, 0x3fb8aa3b, v20
	v_mul_f32_e32 v1, 0x3fb8aa3b, v1
	v_exp_f32_e32 v20, v20
	v_exp_f32_e32 v22, v1
	s_nop 0
	v_pk_mul_f32 v[136:137], v[136:137], v[20:21] op_sel_hi:[1,0]
	v_pk_mul_f32 v[134:135], v[134:135], v[20:21] op_sel_hi:[1,0]
	v_pk_fma_f32 v[4:5], v[4:5], v[22:23], v[136:137] op_sel_hi:[1,0,1]
	v_pk_fma_f32 v[2:3], v[2:3], v[22:23], v[134:135] op_sel_hi:[1,0,1]
	v_mov_b32_e32 v1, v23
	global_store_dwordx4 v[40:41], v[2:5], off offset:3584
	v_add_f32_e32 v1, v1, v101
	v_max_f32_e32 v20, v109, v109
	v_max_f32_e32 v23, v1, v20
	v_sub_f32_e32 v20, v109, v23
	v_sub_f32_e32 v1, v1, v23
	v_mul_f32_e32 v20, 0x3fb8aa3b, v20
	v_mul_f32_e32 v1, 0x3fb8aa3b, v1
	v_exp_f32_e32 v20, v20
	v_exp_f32_e32 v22, v1
	s_nop 0
	v_pk_mul_f32 v[140:141], v[140:141], v[20:21] op_sel_hi:[1,0]
	v_pk_mul_f32 v[138:139], v[138:139], v[20:21] op_sel_hi:[1,0]
	v_pk_fma_f32 v[4:5], v[4:5], v[22:23], v[140:141] op_sel_hi:[1,0,1]
	v_pk_fma_f32 v[2:3], v[2:3], v[22:23], v[138:139] op_sel_hi:[1,0,1]
	v_mov_b32_e32 v1, v23
	v_lshl_add_u64 v[40:41], v[40:41], 0, s[6:7]
	v_lshl_add_u64 v[40:41], v[40:41], 0, s[6:7]
